# speedup vs baseline: 1.0168x; 1.0168x over previous
.Lp3_nopf:
.Lp3_nobar:
	v_lshl_add_u32 v6, v137, 1, v135
	ds_read_b128 v[2:5], v6
	ds_read_b128 v[6:9], v6 offset:16
	v_pk_fma_f32 v[10:11], v[94:95], v[86:87], v[10:11]
	v_pk_fma_f32 v[12:13], v[94:95], v[88:89], v[128:129]
	v_pk_fma_f32 v[14:15], v[94:95], v[82:83], v[36:37]
	s_waitcnt lgkmcnt(1)
	v_fma_mix_f32 v10, v2, 1.0, v10 op_sel_hi:[1,0,0]
	v_fma_mix_f32 v11, v2, 1.0, v11 op_sel:[1,0,0] op_sel_hi:[1,0,0]
	v_fma_mix_f32 v12, v3, 1.0, v12 op_sel_hi:[1,0,0]
	v_fma_mix_f32 v13, v3, 1.0, v13 op_sel:[1,0,0] op_sel_hi:[1,0,0]
	ds_write_b128 v136, v[10:13]
	v_fma_mix_f32 v2, v4, 1.0, v14 op_sel_hi:[1,0,0]
	v_fma_mix_f32 v3, v4, 1.0, v15 op_sel:[1,0,0] op_sel_hi:[1,0,0]
	v_pk_fma_f32 v[10:11], v[94:95], v[84:85], v[38:39]
	v_fma_mix_f32 v4, v5, 1.0, v10 op_sel_hi:[1,0,0]
	v_fma_mix_f32 v5, v5, 1.0, v11 op_sel:[1,0,0] op_sel_hi:[1,0,0]
	ds_write_b128 v136, v[2:5] offset:16
	v_pk_fma_f32 v[10:11], v[94:95], v[78:79], v[40:41]
	v_pk_fma_f32 v[12:13], v[94:95], v[80:81], v[42:43]
	v_pk_fma_f32 v[2:3], v[94:95], v[74:75], v[44:45]
	v_pk_fma_f32 v[4:5], v[94:95], v[76:77], v[46:47]
	s_waitcnt lgkmcnt(2)
	v_fma_mix_f32 v10, v6, 1.0, v10 op_sel_hi:[1,0,0]
	v_fma_mix_f32 v11, v6, 1.0, v11 op_sel:[1,0,0] op_sel_hi:[1,0,0]
	v_fma_mix_f32 v12, v7, 1.0, v12 op_sel_hi:[1,0,0]
	v_fma_mix_f32 v13, v7, 1.0, v13 op_sel:[1,0,0] op_sel_hi:[1,0,0]
	ds_write_b128 v136, v[10:13] offset:32
	v_fma_mix_f32 v2, v8, 1.0, v2 op_sel_hi:[1,0,0]
	v_fma_mix_f32 v3, v8, 1.0, v3 op_sel:[1,0,0] op_sel_hi:[1,0,0]
	v_fma_mix_f32 v4, v9, 1.0, v4 op_sel_hi:[1,0,0]
	v_fma_mix_f32 v5, v9, 1.0, v5 op_sel:[1,0,0] op_sel_hi:[1,0,0]
	ds_write_b128 v136, v[2:5] offset:48
	v_mov_b64_e32 v[92:93], v[64:65]
	v_mov_b64_e32 v[18:19], v[58:59]
	s_movk_i32 s6, 0x80
	s_mov_b64 s[0:1], 0
	s_andn2_b64 vcc, exec, s[2:3]
	v_mov_b32_e32 v138, v133
	v_mov_b32_e32 v139, v132
	v_mov_b64_e32 v[90:91], v[62:63]
	v_mov_b64_e32 v[20:21], v[60:61]
	s_cbranch_vccz .LBB3_19
